# v33: v27 + SwiGLU epilogue VALU trim (log2e folded into col scales, neg modifier on exp) + diff M-block reorder (QK^T between PV halves) + 4-way ILP max tree in both attention loops
# speedup vs baseline: 1.0082x; 1.0082x over previous
.LBB0_1042:
	v_max3_f32 v90, v50, v51, v52
	v_max3_f32 v91, v53, v54, v55
	v_max3_f32 v92, v56, v57, v58
	v_max3_f32 v93, v59, v60, v61
	v_max3_f32 v90, v90, v62, v63
	v_max3_f32 v91, v91, v64, v65
	v_max3_f32 v92, v92, v34, v35
	v_max3_f32 v93, v93, v36, v37
	v_max3_f32 v90, v90, v38, v39
	v_max3_f32 v91, v91, v40, v41
	v_max3_f32 v92, v92, v42, v43
	v_max3_f32 v93, v93, v44, v45
	v_max3_f32 v90, v90, v46, v47
	v_max3_f32 v91, v91, v48, v49
	v_max3_f32 v90, v90, v92, v93
	v_max_f32_e32 v90, v90, v91
	v_mov_b32_e32 v91, v90
	s_nop 1
	v_permlane32_swap_b32_e32 v90, v91
	s_cmp_eq_u32 s86, 1
	s_cselect_b64 s[12:13], -1, 0
	s_cmp_lg_u32 s86, 1
	v_max_f32_e32 v91, v90, v91
	s_cbranch_scc0 .LBB0_1060
	s_mov_b32 s14, 0x41000000
	v_cmp_ge_f32_e32 vcc, s14, v91
	s_cmp_lg_u64 vcc, exec
	s_mov_b64 s[16:17], 0
	s_mov_b64 s[14:15], 0
	s_cbranch_scc0 .LBB0_1057
	v_max_f32_e32 v90, 0, v91
	s_mov_b64 s[14:15], -1
	s_and_b64 vcc, exec, s[16:17]
	s_cbranch_vccz .LBB0_1061
	s_branch .LBB0_1058

.LBB0_1087:
	v_mov_b32_e32 v14, v1
	v_mov_b32_e32 v15, v1
	s_waitcnt vmcnt(0)
	v_sub_u32_e32 v16, v188, v0
	v_mov_b32_e32 v0, v1
	v_mov_b32_e32 v2, v1
	v_mov_b32_e32 v3, v1
	v_mov_b32_e32 v4, v1
	v_mov_b32_e32 v5, v1
	v_mov_b32_e32 v6, v1
	v_mov_b32_e32 v7, v1
	v_mov_b32_e32 v8, v1
	v_mov_b32_e32 v9, v1
	v_mov_b32_e32 v10, v1
	v_mov_b32_e32 v11, v1
	v_mov_b32_e32 v12, v1
	v_mov_b32_e32 v13, v1
	v_mov_b64_e32 v[64:65], v[14:15]
	v_mov_b64_e32 v[48:49], v[14:15]
	v_mov_b64_e32 v[32:33], v[14:15]
	v_cmp_lt_i32_e64 s[82:83], s79, v16
	v_mov_b64_e32 v[62:63], v[12:13]
	v_mov_b64_e32 v[60:61], v[10:11]
	v_mov_b64_e32 v[58:59], v[8:9]
	v_mov_b64_e32 v[56:57], v[6:7]
	v_mov_b64_e32 v[54:55], v[4:5]
	v_mov_b64_e32 v[52:53], v[2:3]
	v_mov_b64_e32 v[50:51], v[0:1]
	v_mov_b64_e32 v[46:47], v[12:13]
	v_mov_b64_e32 v[44:45], v[10:11]
	v_mov_b64_e32 v[42:43], v[8:9]
	v_mov_b64_e32 v[40:41], v[6:7]
	v_mov_b64_e32 v[38:39], v[4:5]
	v_mov_b64_e32 v[36:37], v[2:3]
	v_mov_b64_e32 v[34:35], v[0:1]
	v_mov_b64_e32 v[30:31], v[12:13]
	v_mov_b64_e32 v[28:29], v[10:11]
	v_mov_b64_e32 v[26:27], v[8:9]
	v_mov_b64_e32 v[24:25], v[6:7]
	v_mov_b64_e32 v[22:23], v[4:5]
	v_mov_b64_e32 v[20:21], v[2:3]
	v_mov_b64_e32 v[18:19], v[0:1]
	v_mov_b64_e32 v[16:17], v[14:15]
	s_xor_b64 s[2:3], s[12:13], -1
	s_mov_b32 s88, 0
	v_mov_b32_e32 v165, 0
	s_movk_i32 s89, 0x6000
	s_mov_b32 s78, 1
	s_mov_b32 s93, 63
	v_mov_b32_e32 v167, v198
	v_mov_b32_e32 v169, v197
	s_mov_b64 s[94:95], s[86:87]
	v_mov_b64_e32 v[14:15], v[12:13]
	v_mov_b64_e32 v[12:13], v[10:11]
	v_mov_b64_e32 v[10:11], v[8:9]
	v_mov_b64_e32 v[8:9], v[6:7]
	v_mov_b64_e32 v[6:7], v[4:5]
	v_mov_b64_e32 v[4:5], v[2:3]
	v_mov_b64_e32 v[2:3], v[0:1]
	v_mov_b32_e32 v171, 0
	global_load_dword v175, v1, s[94:95]
	s_add_i32 s4, s78, 2
	s_min_i32 s4, s4, s81
	v_mad_i64_i32 v[200:201], s[4:5], s4, v235, v[182:183]
	s_and_b32 s4, s89, 0x6000
	s_add_i32 s4, s4, s85
	s_mov_b32 s5, m0
	s_mov_b32 m0, s4
	s_nop 0
	global_load_lds_dwordx4 v[200:201], off
	s_mov_b32 m0, s5
	s_add_i32 s4, s78, 1
	s_min_i32 s5, s4, s81
	s_add_i32 s12, s88, 0x8000
	s_and_b32 s15, s12, 0xc000
	v_mad_i64_i32 v[200:201], s[12:13], s5, v235, v[150:151]
	s_add_i32 s12, s15, s75
	s_mov_b32 s13, m0
	s_mov_b32 m0, s12
	s_nop 0
	global_load_lds_dwordx4 v[200:201], off
	s_mov_b32 m0, s13
	v_mad_i64_i32 v[200:201], s[12:13], s5, v235, v[152:153]
	s_add_i32 s5, s15, s74
	s_mov_b32 s12, m0
	s_mov_b32 m0, s5
	s_nop 0
	global_load_lds_dwordx4 v[200:201], off
	s_mov_b32 m0, s12
.LBB0_1088:
	s_add_i32 s4, s78, 1
	s_sub_i32 s14, s93, 63
	s_cmp_le_i32 s14, s80
	s_cselect_b64 s[76:77], -1, 0
	s_cmp_gt_i32 s14, s80
	s_cbranch_scc1 .LBB0_1096
	v_cndmask_b32_e64 v0, 0, v195, s[82:83]
	v_sub_f32_e32 v0, v165, v0
	s_xor_b64 s[12:13], s[82:83], -1
	v_pk_add_f32 v[66:67], v[66:67], v[0:1] op_sel_hi:[1,0] neg_lo:[0,1] neg_hi:[0,1]
	v_pk_add_f32 v[82:83], v[82:83], v[0:1] op_sel_hi:[1,0] neg_lo:[0,1] neg_hi:[0,1]
	v_pk_add_f32 v[68:69], v[68:69], v[0:1] op_sel_hi:[1,0] neg_lo:[0,1] neg_hi:[0,1]
	v_pk_add_f32 v[84:85], v[84:85], v[0:1] op_sel_hi:[1,0] neg_lo:[0,1] neg_hi:[0,1]
	v_pk_add_f32 v[70:71], v[70:71], v[0:1] op_sel_hi:[1,0] neg_lo:[0,1] neg_hi:[0,1]
	v_pk_add_f32 v[86:87], v[86:87], v[0:1] op_sel_hi:[1,0] neg_lo:[0,1] neg_hi:[0,1]
	v_pk_add_f32 v[72:73], v[72:73], v[0:1] op_sel_hi:[1,0] neg_lo:[0,1] neg_hi:[0,1]
	v_pk_add_f32 v[88:89], v[88:89], v[0:1] op_sel_hi:[1,0] neg_lo:[0,1] neg_hi:[0,1]
	v_pk_add_f32 v[74:75], v[74:75], v[0:1] op_sel_hi:[1,0] neg_lo:[0,1] neg_hi:[0,1]
	v_pk_add_f32 v[90:91], v[90:91], v[0:1] op_sel_hi:[1,0] neg_lo:[0,1] neg_hi:[0,1]
	v_pk_add_f32 v[76:77], v[76:77], v[0:1] op_sel_hi:[1,0] neg_lo:[0,1] neg_hi:[0,1]
	v_pk_add_f32 v[92:93], v[92:93], v[0:1] op_sel_hi:[1,0] neg_lo:[0,1] neg_hi:[0,1]
	v_pk_add_f32 v[78:79], v[78:79], v[0:1] op_sel_hi:[1,0] neg_lo:[0,1] neg_hi:[0,1]
	v_pk_add_f32 v[94:95], v[94:95], v[0:1] op_sel_hi:[1,0] neg_lo:[0,1] neg_hi:[0,1]
	v_pk_add_f32 v[80:81], v[80:81], v[0:1] op_sel_hi:[1,0] neg_lo:[0,1] neg_hi:[0,1]
	s_andn2_b64 vcc, exec, s[12:13]
	v_pk_add_f32 v[96:97], v[96:97], v[0:1] op_sel_hi:[1,0] neg_lo:[0,1] neg_hi:[0,1]
	s_cbranch_vccnz .LBB0_1091
	v_mov_b32_e32 v0, v167
	ds_read_b128 v[114:117], v0
	ds_read_b128 v[118:121], v0 offset:128
	ds_read_b128 v[122:125], v0 offset:32
	ds_read_b128 v[126:129], v0 offset:160
	s_waitcnt lgkmcnt(3)
	v_sub_u32_e32 v114, v187, v114
	v_sub_u32_e32 v115, v187, v115
	s_waitcnt lgkmcnt(2)
	v_sub_u32_e32 v118, v187, v118
	v_med3_i32 v114, v114, 0, v241
	v_med3_i32 v115, v115, 0, v241
	v_sub_u32_e32 v119, v187, v119
	v_sub_u32_e32 v116, v187, v116
	v_sub_u32_e32 v120, v187, v120
	v_sub_u32_e32 v117, v187, v117
	v_sub_u32_e32 v121, v187, v121
	v_med3_i32 v118, v118, 0, v241
	v_lshl_add_u32 v114, v114, 2, s92
	v_med3_i32 v119, v119, 0, v241
	v_lshl_add_u32 v115, v115, 2, s92
	v_med3_i32 v116, v116, 0, v241
	v_med3_i32 v120, v120, 0, v241
	v_med3_i32 v117, v117, 0, v241
	v_med3_i32 v121, v121, 0, v241
	v_lshl_add_u32 v118, v118, 2, s92
	v_lshl_add_u32 v119, v119, 2, s92
	v_lshl_add_u32 v116, v116, 2, s92
	v_lshl_add_u32 v120, v120, 2, s92
	v_lshl_add_u32 v117, v117, 2, s92
	v_lshl_add_u32 v121, v121, 2, s92
	ds_read_b32 v200, v114
	ds_read_b32 v202, v118
	ds_read_b32 v201, v115
	ds_read_b32 v203, v119
	ds_read_b32 v204, v116
	ds_read_b32 v206, v120
	ds_read_b32 v205, v117
	ds_read_b32 v207, v121
	s_waitcnt lgkmcnt(9)
	v_sub_u32_e32 v114, v187, v122
	s_waitcnt lgkmcnt(8)
	v_sub_u32_e32 v115, v187, v126
	v_med3_i32 v114, v114, 0, v241
	v_med3_i32 v115, v115, 0, v241
	v_lshl_add_u32 v118, v114, 2, s92
	v_lshl_add_u32 v119, v115, 2, s92
	v_sub_u32_e32 v114, v187, v123
	v_sub_u32_e32 v115, v187, v127
	v_med3_i32 v114, v114, 0, v241
	v_med3_i32 v115, v115, 0, v241
	v_lshl_add_u32 v120, v114, 2, s92
	v_lshl_add_u32 v121, v115, 2, s92
	v_sub_u32_e32 v114, v187, v124
	v_sub_u32_e32 v115, v187, v128
	v_med3_i32 v114, v114, 0, v241
	v_med3_i32 v115, v115, 0, v241
	v_lshl_add_u32 v122, v114, 2, s92
	v_lshl_add_u32 v123, v115, 2, s92
	v_sub_u32_e32 v114, v187, v125
	v_sub_u32_e32 v115, v187, v129
	v_med3_i32 v114, v114, 0, v241
	v_med3_i32 v115, v115, 0, v241
	v_lshl_add_u32 v124, v114, 2, s92
	v_lshl_add_u32 v125, v115, 2, s92
	ds_read_b128 v[114:117], v0 offset:64
	ds_read_b32 v208, v118
	ds_read_b32 v210, v119
	ds_read_b32 v209, v120
	ds_read_b32 v211, v121
	ds_read_b32 v212, v122
	ds_read_b32 v214, v123
	ds_read_b32 v213, v124
	ds_read_b32 v215, v125
	ds_read_b128 v[118:121], v0 offset:192
	ds_read_b128 v[122:125], v0 offset:96
	s_waitcnt lgkmcnt(10)
	v_sub_u32_e32 v116, v187, v116
	v_med3_i32 v116, v116, 0, v241
	v_sub_u32_e32 v114, v187, v114
	ds_read_b128 v[126:129], v0 offset:224
	s_waitcnt lgkmcnt(2)
	v_sub_u32_e32 v0, v187, v118
	v_sub_u32_e32 v115, v187, v115
	v_sub_u32_e32 v118, v187, v119
	v_sub_u32_e32 v119, v187, v120
	v_lshl_add_u32 v120, v116, 2, s92
	v_sub_u32_e32 v116, v187, v117
	v_med3_i32 v114, v114, 0, v241
	v_med3_i32 v115, v115, 0, v241
	v_med3_i32 v118, v118, 0, v241
	v_med3_i32 v119, v119, 0, v241
	v_med3_i32 v116, v116, 0, v241
	v_sub_u32_e32 v117, v187, v121
	v_med3_i32 v0, v0, 0, v241
	v_lshl_add_u32 v114, v114, 2, s92
	v_lshl_add_u32 v115, v115, 2, s92
	v_lshl_add_u32 v118, v118, 2, s92
	v_lshl_add_u32 v119, v119, 2, s92
	v_med3_i32 v117, v117, 0, v241
	v_lshl_add_u32 v121, v116, 2, s92
	v_lshl_add_u32 v0, v0, 2, s92
	v_lshl_add_u32 v173, v117, 2, s92
	ds_read_b32 v114, v114
	ds_read_b32 v116, v0
	ds_read_b32 v115, v115
	ds_read_b32 v117, v118
	ds_read_b32 v118, v120
	ds_read_b32 v120, v119
	ds_read_b32 v119, v121
	ds_read_b32 v121, v173
	s_waitcnt lgkmcnt(9)
	v_sub_u32_e32 v0, v187, v122
	s_waitcnt lgkmcnt(8)
	v_sub_u32_e32 v122, v187, v126
	v_sub_u32_e32 v123, v187, v123
	v_sub_u32_e32 v126, v187, v127
	v_sub_u32_e32 v124, v187, v124
	v_sub_u32_e32 v127, v187, v128
	v_sub_u32_e32 v125, v187, v125
	v_sub_u32_e32 v128, v187, v129
	v_med3_i32 v0, v0, 0, v241
	v_med3_i32 v122, v122, 0, v241
	v_med3_i32 v123, v123, 0, v241
	v_med3_i32 v124, v124, 0, v241
	v_med3_i32 v125, v125, 0, v241
	v_med3_i32 v128, v128, 0, v241
	v_lshl_add_u32 v0, v0, 2, s92
	v_lshl_add_u32 v122, v122, 2, s92
	v_med3_i32 v126, v126, 0, v241
	v_lshl_add_u32 v123, v123, 2, s92
	v_med3_i32 v127, v127, 0, v241
	v_lshl_add_u32 v124, v124, 2, s92
	v_lshl_add_u32 v125, v125, 2, s92
	s_waitcnt lgkmcnt(1)
	v_pk_add_f32 v[76:77], v[76:77], v[118:119]
	v_lshl_add_u32 v119, v128, 2, s92
	v_lshl_add_u32 v126, v126, 2, s92
	v_lshl_add_u32 v127, v127, 2, s92
	v_pk_add_f32 v[74:75], v[74:75], v[114:115]
	ds_read_b32 v114, v0
	ds_read_b32 v118, v122
	ds_read_b32 v115, v123
	ds_read_b32 v122, v124
	ds_read_b32 v123, v125
	ds_read_b32 v125, v119
	ds_read_b32 v124, v127
	ds_read_b32 v119, v126
	v_pk_add_f32 v[66:67], v[66:67], v[200:201]
	v_pk_add_f32 v[68:69], v[68:69], v[204:205]
	v_pk_add_f32 v[70:71], v[70:71], v[208:209]
	v_pk_add_f32 v[72:73], v[72:73], v[212:213]
	s_waitcnt lgkmcnt(5)
	v_pk_add_f32 v[78:79], v[78:79], v[114:115]
	s_waitcnt lgkmcnt(3)
	v_pk_add_f32 v[80:81], v[80:81], v[122:123]
	v_pk_add_f32 v[82:83], v[82:83], v[202:203]
	v_pk_add_f32 v[84:85], v[84:85], v[206:207]
	v_pk_add_f32 v[86:87], v[86:87], v[210:211]
	v_pk_add_f32 v[88:89], v[88:89], v[214:215]
	v_pk_add_f32 v[90:91], v[90:91], v[116:117]
	v_pk_add_f32 v[92:93], v[92:93], v[120:121]
	s_waitcnt lgkmcnt(0)
	v_pk_add_f32 v[94:95], v[94:95], v[118:119]
	v_pk_add_f32 v[96:97], v[96:97], v[124:125]

.LBB0_1093:
	v_max3_f32 v0, v66, v67, v68
	v_max3_f32 v114, v69, v70, v71
	v_max3_f32 v115, v72, v73, v74
	v_max3_f32 v116, v75, v76, v77
	v_max3_f32 v0, v0, v78, v79
	v_max3_f32 v114, v114, v80, v81
	v_max3_f32 v115, v115, v82, v83
	v_max3_f32 v116, v116, v84, v85
	v_max3_f32 v0, v0, v86, v87
	v_max3_f32 v114, v114, v88, v89
	v_max3_f32 v115, v115, v90, v91
	v_max3_f32 v116, v116, v92, v93
	v_max3_f32 v0, v0, v94, v95
	v_max3_f32 v114, v114, v96, v97
	v_max3_f32 v0, v0, v115, v116
	v_max_f32_e32 v0, v0, v114
	v_mov_b32_e32 v114, v0
	s_nop 1
	v_permlane32_swap_b32_e32 v0, v114
	s_cmp_eq_u32 s78, 1
	s_cselect_b64 s[12:13], -1, 0
	s_cmp_lg_u32 s78, 1
	v_max_f32_e32 v114, v0, v114
	s_cbranch_scc0 .LBB0_1111
	s_mov_b32 s5, 0x41000000
	v_cmp_ge_f32_e32 vcc, s5, v114
	s_cmp_lg_u64 vcc, exec
	s_mov_b64 s[16:17], 0
	s_mov_b64 s[14:15], 0
	s_cbranch_scc0 .LBB0_1108
	v_max_f32_e32 v0, 0, v114
	s_mov_b64 s[14:15], -1
	s_and_b64 vcc, exec, s[16:17]
	s_cbranch_vccz .LBB0_1112
	s_branch .LBB0_1109

.LBB0_1099:
	s_and_b32 s5, s88, 0xc000
	v_add_u32_e32 v179, s5, v196
	s_add_i32 s5, s89, 0xffffc000
	s_and_b32 s5, s5, 0x6000
	v_add_u32_e32 v177, s5, v191
	ds_read_b64_tr_b16 v[66:67], v179 offset:0
	ds_read_b64_tr_b16 v[68:69], v179 offset:0x800
	ds_read_b64_tr_b16 v[70:71], v179 offset:0x200
	ds_read_b64_tr_b16 v[72:73], v179 offset:0xa00
	ds_read_b64_tr_b16 v[74:75], v179 offset:0x400
	ds_read_b64_tr_b16 v[76:77], v179 offset:0xc00
	ds_read_b64_tr_b16 v[78:79], v179 offset:0x600
	ds_read_b64_tr_b16 v[80:81], v179 offset:0xe00
	ds_read_b64_tr_b16 v[82:83], v179 offset:0x1000
	ds_read_b64_tr_b16 v[84:85], v179 offset:0x1800
	ds_read_b64_tr_b16 v[86:87], v179 offset:0x1200
	ds_read_b64_tr_b16 v[88:89], v179 offset:0x1a00
	ds_read_b64_tr_b16 v[90:91], v179 offset:0x1400
	ds_read_b64_tr_b16 v[92:93], v179 offset:0x1c00
	ds_read_b64_tr_b16 v[94:95], v179 offset:0x1600
	ds_read_b64_tr_b16 v[96:97], v179 offset:0x1e00
	s_waitcnt lgkmcnt(8)
	s_nop 0
	v_mfma_f32_32x32x16_bf16 v[50:65], v[114:117], v[66:69], v[50:65]
	v_mfma_f32_32x32x16_bf16 v[34:49], v[114:117], v[70:73], v[34:49]
	v_mfma_f32_32x32x16_bf16 v[18:33], v[114:117], v[74:77], v[18:33]
	v_mfma_f32_32x32x16_bf16 v[2:17], v[114:117], v[78:81], v[2:17]
	s_cmp_ge_u32 s78, s84
	s_cselect_b64 s[12:13], -1, 0
	s_sub_i32 s5, s93, 30
	s_cmp_gt_i32 s5, s0
	s_cselect_b64 s[14:15], -1, 0
	s_or_b64 s[12:13], s[12:13], s[14:15]
	s_and_b64 vcc, exec, s[12:13]
	s_cbranch_vccnz .Ldiff_noqk
	ds_read_b128 v[200:203], v177
	ds_read_b128 v[204:207], v177 offset:512
	ds_read_b128 v[208:211], v177 offset:2048
	ds_read_b128 v[212:215], v177 offset:2560
	ds_read_b128 v[216:219], v177 offset:4096
	ds_read_b128 v[228:231], v177 offset:4608
	ds_read_b128 v[244:247], v177 offset:6144
	ds_read_b128 v[248:251], v177 offset:6656
	s_waitcnt lgkmcnt(8)
	v_mfma_f32_32x32x16_bf16 v[50:65], v[118:121], v[82:85], v[50:65]
	v_mfma_f32_32x32x16_bf16 v[34:49], v[118:121], v[86:89], v[34:49]
	v_mfma_f32_32x32x16_bf16 v[18:33], v[118:121], v[90:93], v[18:33]
	v_mfma_f32_32x32x16_bf16 v[2:17], v[118:121], v[94:97], v[2:17]
	s_waitcnt vmcnt(3)
	v_sub_u32_e32 v0, v188, v175
	s_waitcnt lgkmcnt(7)
	v_mfma_f32_32x32x16_bf16 v[66:81], v[200:203], v[98:101], 0
	v_cmp_lt_i32_e64 s[82:83], s79, v0
	s_waitcnt lgkmcnt(6)
	v_mfma_f32_32x32x16_bf16 v[82:97], v[204:207], v[98:101], 0
	s_waitcnt lgkmcnt(5)
	v_mfma_f32_32x32x16_bf16 v[66:81], v[208:211], v[102:105], v[66:81]
	s_waitcnt lgkmcnt(4)
	v_mfma_f32_32x32x16_bf16 v[82:97], v[212:215], v[102:105], v[82:97]
	ds_read_b64_tr_b16 v[200:201], v179 offset:0x2000
	ds_read_b64_tr_b16 v[202:203], v179 offset:0x2800
	ds_read_b64_tr_b16 v[204:205], v179 offset:0x2200
	ds_read_b64_tr_b16 v[206:207], v179 offset:0x2a00
	ds_read_b64_tr_b16 v[208:209], v179 offset:0x2400
	ds_read_b64_tr_b16 v[210:211], v179 offset:0x2c00
	ds_read_b64_tr_b16 v[212:213], v179 offset:0x2600
	ds_read_b64_tr_b16 v[214:215], v179 offset:0x2e00
	s_waitcnt lgkmcnt(11)
	v_mfma_f32_32x32x16_bf16 v[66:81], v[216:219], v[106:109], v[66:81]
	s_waitcnt lgkmcnt(10)
	v_mfma_f32_32x32x16_bf16 v[82:97], v[228:231], v[106:109], v[82:97]
	s_waitcnt lgkmcnt(9)
	v_mfma_f32_32x32x16_bf16 v[66:81], v[244:247], v[110:113], v[66:81]
	s_waitcnt lgkmcnt(8)
	v_mfma_f32_32x32x16_bf16 v[82:97], v[248:251], v[110:113], v[82:97]
	ds_read_b64_tr_b16 v[216:217], v179 offset:0x3000
	ds_read_b64_tr_b16 v[218:219], v179 offset:0x3800
	ds_read_b64_tr_b16 v[228:229], v179 offset:0x3200
	ds_read_b64_tr_b16 v[230:231], v179 offset:0x3a00
	ds_read_b64_tr_b16 v[244:245], v179 offset:0x3400
	ds_read_b64_tr_b16 v[246:247], v179 offset:0x3c00
	ds_read_b64_tr_b16 v[248:249], v179 offset:0x3600
	ds_read_b64_tr_b16 v[250:251], v179 offset:0x3e00
	s_branch .Ldiff_pv23
.Ldiff_noqk:
	s_waitcnt lgkmcnt(0)
	v_mfma_f32_32x32x16_bf16 v[50:65], v[118:121], v[82:85], v[50:65]
	v_mfma_f32_32x32x16_bf16 v[34:49], v[118:121], v[86:89], v[34:49]
	v_mfma_f32_32x32x16_bf16 v[18:33], v[118:121], v[90:93], v[18:33]
	v_mfma_f32_32x32x16_bf16 v[2:17], v[118:121], v[94:97], v[2:17]
	ds_read_b64_tr_b16 v[200:201], v179 offset:0x2000
	ds_read_b64_tr_b16 v[202:203], v179 offset:0x2800
	ds_read_b64_tr_b16 v[204:205], v179 offset:0x2200
	ds_read_b64_tr_b16 v[206:207], v179 offset:0x2a00
	ds_read_b64_tr_b16 v[208:209], v179 offset:0x2400
	ds_read_b64_tr_b16 v[210:211], v179 offset:0x2c00
	ds_read_b64_tr_b16 v[212:213], v179 offset:0x2600
	ds_read_b64_tr_b16 v[214:215], v179 offset:0x2e00
	ds_read_b64_tr_b16 v[216:217], v179 offset:0x3000
	ds_read_b64_tr_b16 v[218:219], v179 offset:0x3800
	ds_read_b64_tr_b16 v[228:229], v179 offset:0x3200
	ds_read_b64_tr_b16 v[230:231], v179 offset:0x3a00
	ds_read_b64_tr_b16 v[244:245], v179 offset:0x3400
	ds_read_b64_tr_b16 v[246:247], v179 offset:0x3c00
	ds_read_b64_tr_b16 v[248:249], v179 offset:0x3600
	ds_read_b64_tr_b16 v[250:251], v179 offset:0x3e00
.Ldiff_pv23:
	s_waitcnt lgkmcnt(8)
	v_mfma_f32_32x32x16_bf16 v[50:65], v[122:125], v[200:203], v[50:65]
	v_mfma_f32_32x32x16_bf16 v[34:49], v[122:125], v[204:207], v[34:49]
	v_mfma_f32_32x32x16_bf16 v[18:33], v[122:125], v[208:211], v[18:33]
	v_mfma_f32_32x32x16_bf16 v[2:17], v[122:125], v[212:215], v[2:17]
	s_waitcnt lgkmcnt(0)
	v_mfma_f32_32x32x16_bf16 v[50:65], v[126:129], v[216:219], v[50:65]
	v_mfma_f32_32x32x16_bf16 v[34:49], v[126:129], v[228:231], v[34:49]
	v_mfma_f32_32x32x16_bf16 v[18:33], v[126:129], v[244:247], v[18:33]
	v_mfma_f32_32x32x16_bf16 v[2:17], v[126:129], v[248:251], v[2:17]
.LBB0_1100:
	global_load_dword v175, v1, s[94:95] offset:4
	s_add_i32 s5, s78, 3
	s_min_i32 s5, s5, s81
	v_mad_i64_i32 v[200:201], s[12:13], s5, v235, v[182:183]
	s_add_i32 s5, s89, 0x2000
	s_and_b32 s5, s5, 0x6000
	s_add_i32 s5, s5, s85
	s_mov_b32 s12, m0
	s_mov_b32 m0, s5
	s_nop 0
	global_load_lds_dwordx4 v[200:201], off
	s_mov_b32 m0, s12
	s_add_i32 s5, s78, 2
	s_min_i32 s5, s5, s81
	s_add_i32 s12, s88, 0xc000
	s_and_b32 s15, s12, 0xc000
	v_mad_i64_i32 v[200:201], s[12:13], s5, v235, v[150:151]
	s_add_i32 s12, s15, s75
	s_mov_b32 s13, m0
	s_mov_b32 m0, s12
	s_nop 0
	global_load_lds_dwordx4 v[200:201], off
	s_mov_b32 m0, s13
	v_mad_i64_i32 v[200:201], s[12:13], s5, v235, v[152:153]
	s_add_i32 s5, s15, s74
	s_mov_b32 s12, m0
	s_mov_b32 m0, s5
	s_nop 0
	global_load_lds_dwordx4 v[200:201], off
	s_mov_b32 m0, s12
	s_and_b64 vcc, exec, s[6:7]
	s_cbranch_vccz .LBB0_1107

.LBB0_1104:
	s_add_u32 s94, s94, 4
	s_addc_u32 s95, s95, 0
	s_addk_i32 s89, 0x2000
	s_add_i32 s5, s1, s4
	s_addk_i32 s88, 0x4000
	s_add_i32 s93, s93, 64
	v_subrev_u32_e32 v169, 64, v169
	s_cmp_eq_u32 s5, 1
	v_add_u32_e32 v167, 0x100, v167
	s_cbranch_scc1 .LBB0_1120
	s_mov_b32 s78, s4
	s_branch .LBB0_1088
.LBB0_1107:
	s_waitcnt vmcnt(3) lgkmcnt(0)
	s_barrier
	s_cbranch_execz .LBB0_1103
	s_branch .LBB0_1104

.LBB0_1511:
	s_lshl_b32 s23, s38, 8
	s_add_i32 s23, s23, s87
	s_mul_i32 s37, s65, 0x5800
	s_mul_hi_i32 s29, s65, 0x5800
	s_add_u32 s37, s59, s37
	s_addc_u32 s29, s60, s29
	s_lshl_b32 s40, s36, 8
	s_ashr_i32 s41, s40, 31
	s_lshl_b64 s[40:41], s[40:41], 2
	s_add_u32 s37, s37, s40
	v_mbcnt_lo_u32_b32 v0, -1, 0
	v_mbcnt_hi_u32_b32 v0, -1, v0
	s_addc_u32 s29, s29, s41
	v_lshrrev_b32_e32 v82, 1, v0
	s_lshl_b32 s38, s72, 2
	v_and_or_b32 v160, v0, 15, s23
	v_and_b32_e32 v162, 24, v82
	s_add_u32 s40, s37, s38
	v_ashrrev_i32_e32 v161, 31, v160
	s_addc_u32 s41, s29, 0
	v_lshlrev_b32_e32 v90, 2, v162
	v_lshl_add_u64 v[146:147], v[160:161], 2, s[20:21]
	global_load_dwordx4 v[86:89], v90, s[40:41] offset:16
	global_load_dwordx4 v[94:97], v90, s[40:41]
	global_load_dwordx4 v[82:85], v90, s[40:41] offset:528
	s_nop 0
	global_load_dwordx4 v[90:93], v90, s[40:41] offset:512
	v_cvt_f32_i32_e32 v173, v143
	global_load_dword v170, v[146:147], off
	global_load_dword v158, v[146:147], off offset:64
	global_load_dword v156, v[146:147], off offset:128
	global_load_dword v154, v[146:147], off offset:192
	global_load_dword v152, v[146:147], off offset:512
	global_load_dword v150, v[146:147], off offset:576
	global_load_dword v148, v[146:147], off offset:640
	global_load_dword v0, v[146:147], off offset:704
	v_cvt_f32_i32_e32 v172, v142
	v_cvt_f32_i32_e32 v143, v145
	v_cvt_f32_i32_e32 v142, v144
	s_lshl_b32 s23, s36, 7
	s_or_b32 s23, s23, s72
	v_add_u32_e32 v163, 0xa0, v160
	v_or_b32_e32 v146, s23, v162
	v_cvt_f32_i32_e32 v133, v133
	v_cvt_f32_i32_e32 v132, v132
	v_cvt_f32_i32_e32 v131, v131
	v_cvt_f32_i32_e32 v130, v130
	s_mov_b32 s23, 0xc3e00000
	s_movk_i32 s29, 0xb00
	v_cvt_f32_i32_e32 v127, v127
	v_cvt_f32_i32_e32 v126, v126
	v_ashrrev_i32_e32 v147, 31, v146
	v_cvt_f32_i32_e32 v129, v129
	v_cvt_f32_i32_e32 v128, v128
	v_cvt_f32_i32_e32 v119, v119
	v_cvt_f32_i32_e32 v118, v118
	v_cvt_f32_i32_e32 v121, v121
	v_cvt_f32_i32_e32 v120, v120
	v_cvt_f32_i32_e32 v123, v123
	v_cvt_f32_i32_e32 v122, v122
	v_cvt_f32_i32_e32 v125, v125
	v_cvt_f32_i32_e32 v124, v124
	v_cvt_f32_i32_e32 v115, v115
	v_cvt_f32_i32_e32 v114, v114
	v_cvt_f32_i32_e32 v117, v117
	v_cvt_f32_i32_e32 v116, v116
	v_or_b32_e32 v168, 16, v160
	v_cvt_f32_i32_e32 v111, v111
	v_cvt_f32_i32_e32 v110, v110
	v_cvt_f32_i32_e32 v113, v113
	v_cvt_f32_i32_e32 v112, v112
	v_cvt_f32_i32_e32 v103, v103
	v_cvt_f32_i32_e32 v102, v102
	v_cvt_f32_i32_e32 v105, v105
	v_cvt_f32_i32_e32 v104, v104
	v_cvt_f32_i32_e32 v107, v107
	v_cvt_f32_i32_e32 v106, v106
	v_cvt_f32_i32_e32 v109, v109
	v_cvt_f32_i32_e32 v108, v108
	v_cvt_f32_i32_e32 v99, v99
	v_cvt_f32_i32_e32 v98, v98
	v_cvt_f32_i32_e32 v101, v101
	v_cvt_f32_i32_e32 v100, v100
	v_or_b32_e32 v167, 32, v160
	v_cvt_f32_i32_e32 v79, v79
	v_cvt_f32_i32_e32 v78, v78
	v_cvt_f32_i32_e32 v81, v81
	v_cvt_f32_i32_e32 v80, v80
	v_cvt_f32_i32_e32 v71, v71
	v_cvt_f32_i32_e32 v70, v70
	v_cvt_f32_i32_e32 v73, v73
	v_cvt_f32_i32_e32 v72, v72
	v_cvt_f32_i32_e32 v75, v75
	v_cvt_f32_i32_e32 v74, v74
	v_cvt_f32_i32_e32 v77, v77
	v_cvt_f32_i32_e32 v76, v76
	v_cvt_f32_i32_e32 v67, v67
	v_cvt_f32_i32_e32 v66, v66
	v_cvt_f32_i32_e32 v69, v69
	v_cvt_f32_i32_e32 v68, v68
	v_or_b32_e32 v166, 48, v160
	v_cvt_f32_i32_e32 v63, v63
	v_cvt_f32_i32_e32 v62, v62
	v_cvt_f32_i32_e32 v65, v65
	v_cvt_f32_i32_e32 v64, v64
	v_cvt_f32_i32_e32 v55, v55
	v_cvt_f32_i32_e32 v54, v54
	v_cvt_f32_i32_e32 v57, v57
	s_waitcnt vmcnt(0)
	v_mul_f32_e32 v94, 0x3fb8aa3b, v94
	v_mul_f32_e32 v95, 0x3fb8aa3b, v95
	v_mul_f32_e32 v96, 0x3fb8aa3b, v96
	v_mul_f32_e32 v97, 0x3fb8aa3b, v97
	v_mul_f32_e32 v86, 0x3fb8aa3b, v86
	v_mul_f32_e32 v87, 0x3fb8aa3b, v87
	v_mul_f32_e32 v88, 0x3fb8aa3b, v88
	v_mul_f32_e32 v89, 0x3fb8aa3b, v89
	v_mul_f32_e32 v90, 0x3f317218, v90
	v_mul_f32_e32 v91, 0x3f317218, v91
	v_mul_f32_e32 v92, 0x3f317218, v92
	v_mul_f32_e32 v93, 0x3f317218, v93
	v_mul_f32_e32 v82, 0x3f317218, v82
	v_mul_f32_e32 v83, 0x3f317218, v83
	v_mul_f32_e32 v84, 0x3f317218, v84
	v_mul_f32_e32 v85, 0x3f317218, v85
	v_pk_mul_f32 v[144:145], v[96:97], v[170:171] op_sel_hi:[1,0]
	v_pk_mul_f32 v[174:175], v[94:95], v[170:171] op_sel_hi:[1,0]
	v_pk_mul_f32 v[142:143], v[144:145], v[142:143]
	v_pk_mul_f32 v[144:145], v[174:175], v[172:173]
	v_cvt_f32_i32_e32 v173, v139
	v_cvt_f32_i32_e32 v172, v138
	v_cvt_f32_i32_e32 v139, v141
	v_cvt_f32_i32_e32 v138, v140
	v_mul_f32_e32 v162, 4.0, v170
	v_pk_mul_f32 v[140:141], v[92:93], v[162:163] op_sel_hi:[1,0]
	v_pk_mul_f32 v[174:175], v[90:91], v[162:163] op_sel_hi:[1,0]
	v_pk_mul_f32 v[138:139], v[140:141], v[138:139]
	v_pk_mul_f32 v[140:141], v[174:175], v[172:173]
	v_cvt_f32_i32_e32 v173, v135
	v_cvt_f32_i32_e32 v172, v134
	v_cvt_f32_i32_e32 v135, v137
	v_cvt_f32_i32_e32 v134, v136
	v_pk_mul_f32 v[136:137], v[88:89], v[170:171] op_sel_hi:[1,0]
	v_pk_mul_f32 v[170:171], v[86:87], v[170:171] op_sel_hi:[1,0]
	v_pk_mul_f32 v[134:135], v[136:137], v[134:135]
	v_pk_mul_f32 v[136:137], v[170:171], v[172:173]
	v_pk_mul_f32 v[170:171], v[84:85], v[162:163] op_sel_hi:[1,0]
	v_pk_mul_f32 v[172:173], v[82:83], v[162:163] op_sel_hi:[1,0]
	v_pk_mul_f32 v[132:133], v[170:171], v[132:133]
	v_pk_mul_f32 v[130:131], v[172:173], v[130:131]
	v_exp_f32_e64 v162, -v144
	v_exp_f32_e64 v170, -v142
	v_exp_f32_e64 v169, -v145
	v_exp_f32_e64 v171, -v143
	v_exp_f32_e64 v172, -v136
	v_exp_f32_e64 v174, -v134
	v_exp_f32_e64 v173, -v137
	v_exp_f32_e64 v175, -v135
	v_add_f32_e32 v162, 1.0, v162
	v_add_f32_e32 v170, 1.0, v170
	v_rcp_f32_e32 v162, v162
	v_add_f32_e32 v169, 1.0, v169
	v_rcp_f32_e32 v170, v170
	v_add_f32_e32 v171, 1.0, v171
	v_add_f32_e32 v172, 1.0, v172
	v_add_f32_e32 v174, 1.0, v174
	v_rcp_f32_e32 v169, v169
	v_rcp_f32_e32 v171, v171
	v_rcp_f32_e32 v172, v172
	v_add_f32_e32 v173, 1.0, v173
	v_rcp_f32_e32 v174, v174
	v_add_f32_e32 v175, 1.0, v175
	v_rcp_f32_e32 v173, v173
	v_rcp_f32_e32 v175, v175
	v_mul_f32_e32 v144, v144, v162
	v_mul_f32_e32 v142, v142, v170
	v_mul_f32_e32 v140, v140, v144
	v_mul_f32_e32 v144, v145, v169
	v_mul_f32_e32 v138, v138, v142
	v_mul_f32_e32 v142, v143, v171
	v_mul_f32_e32 v136, v136, v172
	v_mul_f32_e32 v134, v134, v174
	v_mul_f32_e32 v141, v141, v144
	v_mul_f32_e32 v139, v139, v142
	v_mul_f32_e32 v130, v130, v136
	v_mul_f32_e32 v136, v137, v173
	v_mul_f32_e32 v134, v132, v134
	v_mul_f32_e32 v132, v135, v175
	v_mov_b32_e32 v142, 0x43e00000
	v_mul_f32_e32 v131, v131, v136
	v_mul_f32_e32 v133, v133, v132
	v_med3_f32 v135, v140, s23, v142
	v_med3_f32 v136, v141, s23, v142
	v_cvt_pk_fp8_f32 v132, v135, v136
	v_med3_f32 v130, v130, s23, v142
	v_med3_f32 v131, v131, s23, v142
	v_med3_f32 v135, v133, s23, v142
	v_cvt_pk_fp8_f32 v133, v130, v131
	v_med3_f32 v137, v138, s23, v142
	v_med3_f32 v138, v139, s23, v142
	v_med3_f32 v134, v134, s23, v142
	v_cvt_pk_fp8_f32 v132, v137, v138 op_sel:[0,0,1]
	v_cvt_pk_fp8_f32 v133, v134, v135 op_sel:[0,0,1]
	v_mov_b64_e32 v[130:131], s[18:19]
	v_mad_i64_i32 v[134:135], s[36:37], v160, s29, v[130:131]
	v_lshl_add_u64 v[134:135], v[134:135], 0, v[146:147]
	global_store_dwordx2 v[134:135], v[132:133], off
	v_mul_f32_e32 v132, 4.0, v158
	v_pk_mul_f32 v[136:137], v[94:95], v[158:159] op_sel_hi:[1,0]
	v_pk_mul_f32 v[134:135], v[96:97], v[158:159] op_sel_hi:[1,0]
	v_pk_mul_f32 v[126:127], v[136:137], v[126:127]
	v_pk_mul_f32 v[136:137], v[90:91], v[132:133] op_sel_hi:[1,0]
	v_pk_mul_f32 v[128:129], v[134:135], v[128:129]
	v_pk_mul_f32 v[134:135], v[92:93], v[132:133] op_sel_hi:[1,0]
	v_pk_mul_f32 v[118:119], v[136:137], v[118:119]
	v_pk_mul_f32 v[136:137], v[86:87], v[158:159] op_sel_hi:[1,0]
	v_pk_mul_f32 v[120:121], v[134:135], v[120:121]
	v_pk_mul_f32 v[134:135], v[88:89], v[158:159] op_sel_hi:[1,0]
	v_pk_mul_f32 v[122:123], v[136:137], v[122:123]
	v_pk_mul_f32 v[124:125], v[134:135], v[124:125]
	v_pk_mul_f32 v[134:135], v[84:85], v[132:133] op_sel_hi:[1,0]
	v_pk_mul_f32 v[132:133], v[82:83], v[132:133] op_sel_hi:[1,0]
	v_pk_mul_f32 v[114:115], v[132:133], v[114:115]
	v_exp_f32_e64 v136, -v122
	v_exp_f32_e64 v132, -v126
	v_exp_f32_e64 v137, -v123
	v_exp_f32_e64 v133, -v127
	v_exp_f32_e64 v138, -v124
	v_exp_f32_e64 v139, -v125
	v_add_f32_e32 v136, 1.0, v136
	v_pk_mul_f32 v[116:117], v[134:135], v[116:117]
	v_add_f32_e32 v132, 1.0, v132
	v_rcp_f32_e32 v136, v136
	v_add_f32_e32 v137, 1.0, v137
	v_exp_f32_e64 v134, -v128
	v_rcp_f32_e32 v132, v132
	v_add_f32_e32 v133, 1.0, v133
	v_rcp_f32_e32 v137, v137
	v_add_f32_e32 v138, 1.0, v138
	v_exp_f32_e64 v135, -v129
	v_rcp_f32_e32 v133, v133
	v_rcp_f32_e32 v138, v138
	v_add_f32_e32 v139, 1.0, v139
	v_rcp_f32_e32 v139, v139
	v_mul_f32_e32 v122, v122, v136
	v_add_f32_e32 v134, 1.0, v134
	v_mul_f32_e32 v126, v126, v132
	v_mul_f32_e32 v122, v114, v122
	v_mul_f32_e32 v114, v123, v137
	v_rcp_f32_e32 v134, v134
	v_add_f32_e32 v135, 1.0, v135
	v_mul_f32_e32 v118, v118, v126
	v_mul_f32_e32 v126, v127, v133
	v_mul_f32_e32 v115, v115, v114
	v_mul_f32_e32 v114, v124, v138
	v_rcp_f32_e32 v135, v135
	v_mul_f32_e32 v119, v119, v126
	v_mul_f32_e32 v116, v116, v114
	v_mul_f32_e32 v114, v125, v139
	v_mul_f32_e32 v117, v117, v114
	v_med3_f32 v118, v118, s23, v142
	v_med3_f32 v119, v119, s23, v142
	v_cvt_pk_fp8_f32 v114, v118, v119
	v_med3_f32 v118, v122, s23, v142
	v_med3_f32 v119, v115, s23, v142
	v_mul_f32_e32 v126, v128, v134
	v_cvt_pk_fp8_f32 v115, v118, v119
	v_mul_f32_e32 v120, v120, v126
	v_mul_f32_e32 v126, v129, v135
	v_mul_f32_e32 v121, v121, v126
	v_med3_f32 v120, v120, s23, v142
	v_med3_f32 v121, v121, s23, v142
	v_med3_f32 v116, v116, s23, v142
	v_med3_f32 v117, v117, s23, v142
	v_cvt_pk_fp8_f32 v114, v120, v121 op_sel:[0,0,1]
	v_cvt_pk_fp8_f32 v115, v116, v117 op_sel:[0,0,1]
	v_mad_i64_i32 v[116:117], s[36:37], v168, s29, v[130:131]
	v_lshl_add_u64 v[116:117], v[116:117], 0, v[146:147]
	global_store_dwordx2 v[116:117], v[114:115], off
	v_mul_f32_e32 v114, 4.0, v156
	v_pk_mul_f32 v[118:119], v[94:95], v[156:157] op_sel_hi:[1,0]
	v_pk_mul_f32 v[116:117], v[96:97], v[156:157] op_sel_hi:[1,0]
	v_pk_mul_f32 v[110:111], v[118:119], v[110:111]
	v_pk_mul_f32 v[118:119], v[90:91], v[114:115] op_sel_hi:[1,0]
	v_pk_mul_f32 v[112:113], v[116:117], v[112:113]
	v_pk_mul_f32 v[116:117], v[92:93], v[114:115] op_sel_hi:[1,0]
	v_pk_mul_f32 v[102:103], v[118:119], v[102:103]
	v_pk_mul_f32 v[118:119], v[86:87], v[156:157] op_sel_hi:[1,0]
	v_pk_mul_f32 v[104:105], v[116:117], v[104:105]
	v_pk_mul_f32 v[116:117], v[88:89], v[156:157] op_sel_hi:[1,0]
	v_pk_mul_f32 v[106:107], v[118:119], v[106:107]
	v_pk_mul_f32 v[108:109], v[116:117], v[108:109]
	v_pk_mul_f32 v[116:117], v[84:85], v[114:115] op_sel_hi:[1,0]
	v_pk_mul_f32 v[114:115], v[82:83], v[114:115] op_sel_hi:[1,0]
	v_pk_mul_f32 v[98:99], v[114:115], v[98:99]
	v_exp_f32_e64 v118, -v106
	v_exp_f32_e64 v114, -v110
	v_exp_f32_e64 v119, -v107
	v_exp_f32_e64 v115, -v111
	v_exp_f32_e64 v120, -v108
	v_exp_f32_e64 v121, -v109
	v_add_f32_e32 v118, 1.0, v118
	v_pk_mul_f32 v[100:101], v[116:117], v[100:101]
	v_add_f32_e32 v114, 1.0, v114
	v_rcp_f32_e32 v118, v118
	v_add_f32_e32 v119, 1.0, v119
	v_exp_f32_e64 v116, -v112
	v_rcp_f32_e32 v114, v114
	v_add_f32_e32 v115, 1.0, v115
	v_rcp_f32_e32 v119, v119
	v_add_f32_e32 v120, 1.0, v120
	v_exp_f32_e64 v117, -v113
	v_rcp_f32_e32 v115, v115
	v_rcp_f32_e32 v120, v120
	v_add_f32_e32 v121, 1.0, v121
	v_rcp_f32_e32 v121, v121
	v_mul_f32_e32 v106, v106, v118
	v_add_f32_e32 v116, 1.0, v116
	v_mul_f32_e32 v110, v110, v114
	v_mul_f32_e32 v106, v98, v106
	v_mul_f32_e32 v98, v107, v119
	v_rcp_f32_e32 v116, v116
	v_add_f32_e32 v117, 1.0, v117
	v_mul_f32_e32 v102, v102, v110
	v_mul_f32_e32 v110, v111, v115
	v_mul_f32_e32 v99, v99, v98
	v_mul_f32_e32 v98, v108, v120
	v_rcp_f32_e32 v117, v117
	v_mul_f32_e32 v103, v103, v110
	v_mul_f32_e32 v100, v100, v98
	v_mul_f32_e32 v98, v109, v121
	v_mul_f32_e32 v101, v101, v98
	v_med3_f32 v102, v102, s23, v142
	v_med3_f32 v103, v103, s23, v142
	v_cvt_pk_fp8_f32 v98, v102, v103
	v_med3_f32 v102, v106, s23, v142
	v_med3_f32 v103, v99, s23, v142
	v_mul_f32_e32 v110, v112, v116
	v_cvt_pk_fp8_f32 v99, v102, v103
	v_mul_f32_e32 v104, v104, v110
	v_mul_f32_e32 v110, v113, v117
	v_mul_f32_e32 v105, v105, v110
	v_med3_f32 v104, v104, s23, v142
	v_med3_f32 v105, v105, s23, v142
	v_med3_f32 v100, v100, s23, v142
	v_med3_f32 v101, v101, s23, v142
	v_cvt_pk_fp8_f32 v98, v104, v105 op_sel:[0,0,1]
	v_cvt_pk_fp8_f32 v99, v100, v101 op_sel:[0,0,1]
	v_mad_i64_i32 v[100:101], s[36:37], v167, s29, v[130:131]
	v_lshl_add_u64 v[100:101], v[100:101], 0, v[146:147]
	global_store_dwordx2 v[100:101], v[98:99], off
	v_mul_f32_e32 v98, 4.0, v154
	v_pk_mul_f32 v[102:103], v[94:95], v[154:155] op_sel_hi:[1,0]
	v_pk_mul_f32 v[100:101], v[96:97], v[154:155] op_sel_hi:[1,0]
	v_pk_mul_f32 v[78:79], v[102:103], v[78:79]
	v_pk_mul_f32 v[102:103], v[90:91], v[98:99] op_sel_hi:[1,0]
	v_pk_mul_f32 v[80:81], v[100:101], v[80:81]
	v_pk_mul_f32 v[100:101], v[92:93], v[98:99] op_sel_hi:[1,0]
	v_pk_mul_f32 v[70:71], v[102:103], v[70:71]
	v_pk_mul_f32 v[102:103], v[86:87], v[154:155] op_sel_hi:[1,0]
	v_pk_mul_f32 v[72:73], v[100:101], v[72:73]
	v_pk_mul_f32 v[100:101], v[88:89], v[154:155] op_sel_hi:[1,0]
	v_pk_mul_f32 v[74:75], v[102:103], v[74:75]
	v_pk_mul_f32 v[76:77], v[100:101], v[76:77]
	v_pk_mul_f32 v[100:101], v[84:85], v[98:99] op_sel_hi:[1,0]
	v_pk_mul_f32 v[98:99], v[82:83], v[98:99] op_sel_hi:[1,0]
	v_pk_mul_f32 v[66:67], v[98:99], v[66:67]
	v_exp_f32_e64 v102, -v74
	v_exp_f32_e64 v98, -v78
	v_exp_f32_e64 v103, -v75
	v_exp_f32_e64 v99, -v79
	v_exp_f32_e64 v104, -v76
	v_exp_f32_e64 v105, -v77
	v_add_f32_e32 v102, 1.0, v102
	v_pk_mul_f32 v[68:69], v[100:101], v[68:69]
	v_add_f32_e32 v98, 1.0, v98
	v_rcp_f32_e32 v102, v102
	v_add_f32_e32 v103, 1.0, v103
	v_exp_f32_e64 v100, -v80
	v_rcp_f32_e32 v98, v98
	v_add_f32_e32 v99, 1.0, v99
	v_rcp_f32_e32 v103, v103
	v_add_f32_e32 v104, 1.0, v104
	v_exp_f32_e64 v101, -v81
	v_rcp_f32_e32 v99, v99
	v_rcp_f32_e32 v104, v104
	v_add_f32_e32 v105, 1.0, v105
	v_rcp_f32_e32 v105, v105
	v_mul_f32_e32 v74, v74, v102
	v_add_f32_e32 v100, 1.0, v100
	v_mul_f32_e32 v78, v78, v98
	v_mul_f32_e32 v74, v66, v74
	v_mul_f32_e32 v66, v75, v103
	v_rcp_f32_e32 v100, v100
	v_add_f32_e32 v101, 1.0, v101
	v_mul_f32_e32 v70, v70, v78
	v_mul_f32_e32 v78, v79, v99
	v_mul_f32_e32 v67, v67, v66
	v_mul_f32_e32 v66, v76, v104
	v_rcp_f32_e32 v101, v101
	v_mul_f32_e32 v71, v71, v78
	v_mul_f32_e32 v68, v68, v66
	v_mul_f32_e32 v66, v77, v105
	v_mul_f32_e32 v69, v69, v66
	v_med3_f32 v70, v70, s23, v142
	v_med3_f32 v71, v71, s23, v142
	v_cvt_pk_fp8_f32 v66, v70, v71
	v_med3_f32 v70, v74, s23, v142
	v_med3_f32 v71, v67, s23, v142
	v_mul_f32_e32 v78, v80, v100
	v_cvt_pk_fp8_f32 v67, v70, v71
	v_mul_f32_e32 v72, v72, v78
	v_mul_f32_e32 v78, v81, v101
	v_mul_f32_e32 v73, v73, v78
	v_med3_f32 v72, v72, s23, v142
	v_med3_f32 v73, v73, s23, v142
	v_med3_f32 v68, v68, s23, v142
	v_med3_f32 v69, v69, s23, v142
	v_cvt_pk_fp8_f32 v66, v72, v73 op_sel:[0,0,1]
	v_cvt_pk_fp8_f32 v67, v68, v69 op_sel:[0,0,1]
	v_mad_i64_i32 v[68:69], s[36:37], v166, s29, v[130:131]
	v_lshl_add_u64 v[68:69], v[68:69], 0, v[146:147]
	v_cvt_f32_i32_e32 v56, v56
	v_cvt_f32_i32_e32 v59, v59
	v_cvt_f32_i32_e32 v58, v58
	global_store_dwordx2 v[68:69], v[66:67], off
	v_mul_f32_e32 v66, 4.0, v152
	v_pk_mul_f32 v[70:71], v[94:95], v[152:153] op_sel_hi:[1,0]
	v_cvt_f32_i32_e32 v61, v61
	v_cvt_f32_i32_e32 v60, v60
	v_pk_mul_f32 v[68:69], v[96:97], v[152:153] op_sel_hi:[1,0]
	v_pk_mul_f32 v[62:63], v[70:71], v[62:63]
	v_pk_mul_f32 v[70:71], v[90:91], v[66:67] op_sel_hi:[1,0]
	v_cvt_f32_i32_e32 v51, v51
	v_cvt_f32_i32_e32 v50, v50
	v_pk_mul_f32 v[64:65], v[68:69], v[64:65]
	v_pk_mul_f32 v[68:69], v[92:93], v[66:67] op_sel_hi:[1,0]
	v_pk_mul_f32 v[54:55], v[70:71], v[54:55]
	v_pk_mul_f32 v[70:71], v[86:87], v[152:153] op_sel_hi:[1,0]
	v_pk_mul_f32 v[56:57], v[68:69], v[56:57]
	v_pk_mul_f32 v[68:69], v[88:89], v[152:153] op_sel_hi:[1,0]
	v_pk_mul_f32 v[58:59], v[70:71], v[58:59]
	v_pk_mul_f32 v[60:61], v[68:69], v[60:61]
	v_pk_mul_f32 v[68:69], v[84:85], v[66:67] op_sel_hi:[1,0]
	v_pk_mul_f32 v[66:67], v[82:83], v[66:67] op_sel_hi:[1,0]
	v_pk_mul_f32 v[50:51], v[66:67], v[50:51]
	v_exp_f32_e64 v70, -v58
	v_cvt_f32_i32_e32 v53, v53
	v_cvt_f32_i32_e32 v52, v52
	v_exp_f32_e64 v66, -v62
	v_exp_f32_e64 v71, -v59
	v_exp_f32_e64 v67, -v63
	v_exp_f32_e64 v72, -v60
	v_exp_f32_e64 v73, -v61
	v_add_f32_e32 v70, 1.0, v70
	v_pk_mul_f32 v[52:53], v[68:69], v[52:53]
	v_add_f32_e32 v66, 1.0, v66
	v_rcp_f32_e32 v70, v70
	v_add_f32_e32 v71, 1.0, v71
	v_exp_f32_e64 v68, -v64
	v_rcp_f32_e32 v66, v66
	v_add_f32_e32 v67, 1.0, v67
	v_rcp_f32_e32 v71, v71
	v_add_f32_e32 v72, 1.0, v72
	v_exp_f32_e64 v69, -v65
	v_rcp_f32_e32 v67, v67
	v_rcp_f32_e32 v72, v72
	v_add_f32_e32 v73, 1.0, v73
	v_rcp_f32_e32 v73, v73
	v_mul_f32_e32 v58, v58, v70
	v_add_f32_e32 v68, 1.0, v68
	v_mul_f32_e32 v62, v62, v66
	v_mul_f32_e32 v58, v50, v58
	v_mul_f32_e32 v50, v59, v71
	v_rcp_f32_e32 v68, v68
	v_add_f32_e32 v69, 1.0, v69
	v_mul_f32_e32 v54, v54, v62
	v_mul_f32_e32 v62, v63, v67
	v_mul_f32_e32 v51, v51, v50
	v_mul_f32_e32 v50, v60, v72
	v_rcp_f32_e32 v69, v69
	v_mul_f32_e32 v55, v55, v62
	v_mul_f32_e32 v52, v52, v50
	v_mul_f32_e32 v50, v61, v73
	v_mul_f32_e32 v53, v53, v50
	v_med3_f32 v54, v54, s23, v142
	v_med3_f32 v55, v55, s23, v142
	v_cvt_pk_fp8_f32 v50, v54, v55
	v_med3_f32 v54, v58, s23, v142
	v_med3_f32 v55, v51, s23, v142
	v_mul_f32_e32 v62, v64, v68
	v_cvt_pk_fp8_f32 v51, v54, v55
	v_mul_f32_e32 v56, v56, v62
	v_mul_f32_e32 v62, v65, v69
	v_mul_f32_e32 v57, v57, v62
	v_med3_f32 v56, v56, s23, v142
	v_med3_f32 v57, v57, s23, v142
	v_med3_f32 v52, v52, s23, v142
	v_med3_f32 v53, v53, s23, v142
	v_cvt_pk_fp8_f32 v50, v56, v57 op_sel:[0,0,1]
	v_cvt_pk_fp8_f32 v51, v52, v53 op_sel:[0,0,1]
	v_add_u32_e32 v165, 0x80, v160
	v_cvt_f32_i32_e32 v47, v47
	v_cvt_f32_i32_e32 v46, v46
	v_mad_i64_i32 v[52:53], s[36:37], v165, s29, v[130:131]
	v_cvt_f32_i32_e32 v49, v49
	v_cvt_f32_i32_e32 v48, v48
	v_cvt_f32_i32_e32 v39, v39
	v_cvt_f32_i32_e32 v38, v38
	v_lshl_add_u64 v[52:53], v[52:53], 0, v[146:147]
	v_cvt_f32_i32_e32 v41, v41
	v_cvt_f32_i32_e32 v40, v40
	v_cvt_f32_i32_e32 v43, v43
	v_cvt_f32_i32_e32 v42, v42
	global_store_dwordx2 v[52:53], v[50:51], off
	v_mul_f32_e32 v50, 4.0, v150
	v_pk_mul_f32 v[54:55], v[94:95], v[150:151] op_sel_hi:[1,0]
	v_cvt_f32_i32_e32 v45, v45
	v_cvt_f32_i32_e32 v44, v44
	v_pk_mul_f32 v[52:53], v[96:97], v[150:151] op_sel_hi:[1,0]
	v_pk_mul_f32 v[46:47], v[54:55], v[46:47]
	v_pk_mul_f32 v[54:55], v[90:91], v[50:51] op_sel_hi:[1,0]
	v_cvt_f32_i32_e32 v35, v35
	v_cvt_f32_i32_e32 v34, v34
	v_pk_mul_f32 v[48:49], v[52:53], v[48:49]
	v_pk_mul_f32 v[52:53], v[92:93], v[50:51] op_sel_hi:[1,0]
	v_pk_mul_f32 v[38:39], v[54:55], v[38:39]
	v_pk_mul_f32 v[54:55], v[86:87], v[150:151] op_sel_hi:[1,0]
	v_pk_mul_f32 v[40:41], v[52:53], v[40:41]
	v_pk_mul_f32 v[52:53], v[88:89], v[150:151] op_sel_hi:[1,0]
	v_pk_mul_f32 v[42:43], v[54:55], v[42:43]
	v_pk_mul_f32 v[44:45], v[52:53], v[44:45]
	v_pk_mul_f32 v[52:53], v[84:85], v[50:51] op_sel_hi:[1,0]
	v_pk_mul_f32 v[50:51], v[82:83], v[50:51] op_sel_hi:[1,0]
	v_pk_mul_f32 v[34:35], v[50:51], v[34:35]
	v_exp_f32_e64 v54, -v42
	v_cvt_f32_i32_e32 v37, v37
	v_cvt_f32_i32_e32 v36, v36
	v_exp_f32_e64 v50, -v46
	v_exp_f32_e64 v55, -v43
	v_exp_f32_e64 v51, -v47
	v_exp_f32_e64 v56, -v44
	v_exp_f32_e64 v57, -v45
	v_add_f32_e32 v54, 1.0, v54
	v_pk_mul_f32 v[36:37], v[52:53], v[36:37]
	v_add_f32_e32 v50, 1.0, v50
	v_rcp_f32_e32 v54, v54
	v_add_f32_e32 v55, 1.0, v55
	v_exp_f32_e64 v52, -v48
	v_rcp_f32_e32 v50, v50
	v_add_f32_e32 v51, 1.0, v51
	v_rcp_f32_e32 v55, v55
	v_add_f32_e32 v56, 1.0, v56
	v_exp_f32_e64 v53, -v49
	v_rcp_f32_e32 v51, v51
	v_rcp_f32_e32 v56, v56
	v_add_f32_e32 v57, 1.0, v57
	v_rcp_f32_e32 v57, v57
	v_mul_f32_e32 v42, v42, v54
	v_add_f32_e32 v52, 1.0, v52
	v_mul_f32_e32 v46, v46, v50
	v_mul_f32_e32 v42, v34, v42
	v_mul_f32_e32 v34, v43, v55
	v_rcp_f32_e32 v52, v52
	v_add_f32_e32 v53, 1.0, v53
	v_mul_f32_e32 v38, v38, v46
	v_mul_f32_e32 v46, v47, v51
	v_mul_f32_e32 v35, v35, v34
	v_mul_f32_e32 v34, v44, v56
	v_rcp_f32_e32 v53, v53
	v_mul_f32_e32 v39, v39, v46
	v_mul_f32_e32 v36, v36, v34
	v_mul_f32_e32 v34, v45, v57
	v_mul_f32_e32 v37, v37, v34
	v_med3_f32 v38, v38, s23, v142
	v_med3_f32 v39, v39, s23, v142
	v_cvt_pk_fp8_f32 v34, v38, v39
	v_med3_f32 v38, v42, s23, v142
	v_med3_f32 v39, v35, s23, v142
	v_mul_f32_e32 v46, v48, v52
	v_cvt_pk_fp8_f32 v35, v38, v39
	v_mul_f32_e32 v40, v40, v46
	v_mul_f32_e32 v46, v49, v53
	v_mul_f32_e32 v41, v41, v46
	v_med3_f32 v40, v40, s23, v142
	v_med3_f32 v41, v41, s23, v142
	v_med3_f32 v36, v36, s23, v142
	v_med3_f32 v37, v37, s23, v142
	v_cvt_pk_fp8_f32 v34, v40, v41 op_sel:[0,0,1]
	v_cvt_pk_fp8_f32 v35, v36, v37 op_sel:[0,0,1]
	v_add_u32_e32 v164, 0x90, v160
	v_cvt_f32_i32_e32 v31, v31
	v_cvt_f32_i32_e32 v30, v30
	v_mad_i64_i32 v[36:37], s[36:37], v164, s29, v[130:131]
	v_cvt_f32_i32_e32 v33, v33
	v_cvt_f32_i32_e32 v32, v32
	v_cvt_f32_i32_e32 v23, v23
	v_cvt_f32_i32_e32 v22, v22
	v_lshl_add_u64 v[36:37], v[36:37], 0, v[146:147]
	v_cvt_f32_i32_e32 v25, v25
	v_cvt_f32_i32_e32 v24, v24
	v_cvt_f32_i32_e32 v27, v27
	v_cvt_f32_i32_e32 v26, v26
	global_store_dwordx2 v[36:37], v[34:35], off
	v_mul_f32_e32 v34, 4.0, v148
	v_pk_mul_f32 v[38:39], v[94:95], v[148:149] op_sel_hi:[1,0]
	v_cvt_f32_i32_e32 v29, v29
	v_cvt_f32_i32_e32 v28, v28
	v_pk_mul_f32 v[36:37], v[96:97], v[148:149] op_sel_hi:[1,0]
	v_pk_mul_f32 v[30:31], v[38:39], v[30:31]
	v_pk_mul_f32 v[38:39], v[90:91], v[34:35] op_sel_hi:[1,0]
	v_cvt_f32_i32_e32 v19, v19
	v_cvt_f32_i32_e32 v18, v18
	v_pk_mul_f32 v[32:33], v[36:37], v[32:33]
	v_pk_mul_f32 v[36:37], v[92:93], v[34:35] op_sel_hi:[1,0]
	v_pk_mul_f32 v[22:23], v[38:39], v[22:23]
	v_pk_mul_f32 v[38:39], v[86:87], v[148:149] op_sel_hi:[1,0]
	v_pk_mul_f32 v[24:25], v[36:37], v[24:25]
	v_pk_mul_f32 v[36:37], v[88:89], v[148:149] op_sel_hi:[1,0]
	v_pk_mul_f32 v[26:27], v[38:39], v[26:27]
	v_pk_mul_f32 v[28:29], v[36:37], v[28:29]
	v_pk_mul_f32 v[36:37], v[84:85], v[34:35] op_sel_hi:[1,0]
	v_pk_mul_f32 v[34:35], v[82:83], v[34:35] op_sel_hi:[1,0]
	v_pk_mul_f32 v[18:19], v[34:35], v[18:19]
	v_exp_f32_e64 v38, -v26
	v_cvt_f32_i32_e32 v21, v21
	v_cvt_f32_i32_e32 v20, v20
	v_exp_f32_e64 v34, -v30
	v_exp_f32_e64 v39, -v27
	v_exp_f32_e64 v35, -v31
	v_exp_f32_e64 v40, -v28
	v_exp_f32_e64 v41, -v29
	v_add_f32_e32 v38, 1.0, v38
	v_pk_mul_f32 v[20:21], v[36:37], v[20:21]
	v_add_f32_e32 v34, 1.0, v34
	v_rcp_f32_e32 v38, v38
	v_add_f32_e32 v39, 1.0, v39
	v_exp_f32_e64 v36, -v32
	v_rcp_f32_e32 v34, v34
	v_add_f32_e32 v35, 1.0, v35
	v_rcp_f32_e32 v39, v39
	v_add_f32_e32 v40, 1.0, v40
	v_exp_f32_e64 v37, -v33
	v_rcp_f32_e32 v35, v35
	v_rcp_f32_e32 v40, v40
	v_add_f32_e32 v41, 1.0, v41
	v_rcp_f32_e32 v41, v41
	v_mul_f32_e32 v26, v26, v38
	v_add_f32_e32 v36, 1.0, v36
	v_mul_f32_e32 v30, v30, v34
	v_mul_f32_e32 v26, v18, v26
	v_mul_f32_e32 v18, v27, v39
	v_rcp_f32_e32 v36, v36
	v_add_f32_e32 v37, 1.0, v37
	v_mul_f32_e32 v22, v22, v30
	v_mul_f32_e32 v30, v31, v35
	v_mul_f32_e32 v19, v19, v18
	v_mul_f32_e32 v18, v28, v40
	v_rcp_f32_e32 v37, v37
	v_mul_f32_e32 v23, v23, v30
	v_mul_f32_e32 v20, v20, v18
	v_mul_f32_e32 v18, v29, v41
	v_mul_f32_e32 v21, v21, v18
	v_med3_f32 v22, v22, s23, v142
	v_med3_f32 v23, v23, s23, v142
	v_cvt_pk_fp8_f32 v18, v22, v23
	v_med3_f32 v22, v26, s23, v142
	v_med3_f32 v23, v19, s23, v142
	v_mul_f32_e32 v30, v32, v36
	v_cvt_pk_fp8_f32 v19, v22, v23
	v_mul_f32_e32 v24, v24, v30
	v_mul_f32_e32 v30, v33, v37
	v_mul_f32_e32 v25, v25, v30
	v_med3_f32 v24, v24, s23, v142
	v_med3_f32 v25, v25, s23, v142
	v_med3_f32 v20, v20, s23, v142
	v_med3_f32 v21, v21, s23, v142
	v_cvt_pk_fp8_f32 v18, v24, v25 op_sel:[0,0,1]
	v_cvt_pk_fp8_f32 v19, v20, v21 op_sel:[0,0,1]
	v_cvt_f32_i32_e32 v17, v17
	v_cvt_f32_i32_e32 v16, v16
	v_mad_i64_i32 v[20:21], s[36:37], v163, s29, v[130:131]
	v_cvt_f32_i32_e32 v15, v15
	v_cvt_f32_i32_e32 v14, v14
	v_cvt_f32_i32_e32 v9, v9
	v_cvt_f32_i32_e32 v8, v8
	v_lshl_add_u64 v[20:21], v[20:21], 0, v[146:147]
	v_cvt_f32_i32_e32 v7, v7
	v_cvt_f32_i32_e32 v6, v6
	v_cvt_f32_i32_e32 v13, v13
	v_cvt_f32_i32_e32 v12, v12
	global_store_dwordx2 v[20:21], v[18:19], off
	v_mul_f32_e32 v18, 4.0, v0
	v_pk_mul_f32 v[20:21], v[96:97], v[0:1] op_sel_hi:[1,0]
	v_cvt_f32_i32_e32 v3, v3
	v_cvt_f32_i32_e32 v2, v2
	v_pk_mul_f32 v[22:23], v[94:95], v[0:1] op_sel_hi:[1,0]
	v_pk_mul_f32 v[16:17], v[20:21], v[16:17]
	v_pk_mul_f32 v[20:21], v[92:93], v[18:19] op_sel_hi:[1,0]
	v_pk_mul_f32 v[14:15], v[22:23], v[14:15]
	v_pk_mul_f32 v[22:23], v[90:91], v[18:19] op_sel_hi:[1,0]
	v_pk_mul_f32 v[8:9], v[20:21], v[8:9]
	v_cvt_f32_i32_e32 v11, v11
	v_cvt_f32_i32_e32 v10, v10
	v_pk_mul_f32 v[20:21], v[88:89], v[0:1] op_sel_hi:[1,0]
	v_cvt_f32_i32_e32 v5, v5
	v_cvt_f32_i32_e32 v4, v4
	v_pk_mul_f32 v[6:7], v[22:23], v[6:7]
	v_pk_mul_f32 v[22:23], v[86:87], v[0:1] op_sel_hi:[1,0]
	v_pk_mul_f32 v[12:13], v[20:21], v[12:13]
	v_pk_mul_f32 v[20:21], v[84:85], v[18:19] op_sel_hi:[1,0]
	v_pk_mul_f32 v[18:19], v[82:83], v[18:19] op_sel_hi:[1,0]
	v_pk_mul_f32 v[2:3], v[18:19], v[2:3]
	v_exp_f32_e64 v0, -v14
	v_exp_f32_e64 v18, -v15
	v_pk_mul_f32 v[10:11], v[22:23], v[10:11]
	v_pk_mul_f32 v[4:5], v[20:21], v[4:5]
	v_exp_f32_e64 v19, -v16
	v_exp_f32_e64 v20, -v17
	v_exp_f32_e64 v21, -v10
	v_add_f32_e32 v0, 1.0, v0
	v_exp_f32_e64 v22, -v11
	v_rcp_f32_e32 v0, v0
	v_add_f32_e32 v18, 1.0, v18
	v_exp_f32_e64 v23, -v12
	v_rcp_f32_e32 v18, v18
	v_add_f32_e32 v19, 1.0, v19
	v_exp_f32_e64 v24, -v13
	v_rcp_f32_e32 v19, v19
	v_add_f32_e32 v20, 1.0, v20
	v_rcp_f32_e32 v20, v20
	v_add_f32_e32 v21, 1.0, v21
	v_rcp_f32_e32 v21, v21
	v_add_f32_e32 v22, 1.0, v22
	v_mul_f32_e32 v0, v14, v0
	v_rcp_f32_e32 v22, v22
	v_add_f32_e32 v23, 1.0, v23
	v_mul_f32_e32 v0, v6, v0
	v_mul_f32_e32 v6, v15, v18
	v_rcp_f32_e32 v23, v23
	v_add_f32_e32 v24, 1.0, v24
	v_mul_f32_e32 v6, v7, v6
	v_mul_f32_e32 v7, v16, v19
	v_rcp_f32_e32 v24, v24
	v_mul_f32_e32 v7, v8, v7
	v_mul_f32_e32 v8, v17, v20
	v_mul_f32_e32 v8, v9, v8
	v_mul_f32_e32 v9, v10, v21
	v_mul_f32_e32 v9, v2, v9
	v_mul_f32_e32 v2, v11, v22
	v_mul_f32_e32 v3, v3, v2
	v_mul_f32_e32 v2, v12, v23
	v_mul_f32_e32 v4, v4, v2
	v_mul_f32_e32 v2, v13, v24
	v_mul_f32_e32 v5, v5, v2
	v_med3_f32 v0, v0, s23, v142
	v_med3_f32 v6, v6, s23, v142
	v_cvt_pk_fp8_f32 v2, v0, v6
	v_med3_f32 v0, v9, s23, v142
	v_med3_f32 v6, v3, s23, v142
	v_cvt_pk_fp8_f32 v3, v0, v6
	v_med3_f32 v7, v7, s23, v142
	v_med3_f32 v8, v8, s23, v142
	v_med3_f32 v4, v4, s23, v142
	v_med3_f32 v5, v5, s23, v142
	v_cvt_pk_fp8_f32 v2, v7, v8 op_sel:[0,0,1]
	v_cvt_pk_fp8_f32 v3, v4, v5 op_sel:[0,0,1]
	v_add_u32_e32 v161, 0xb0, v160
	v_mad_i64_i32 v[4:5], s[36:37], v161, s29, v[130:131]
	v_lshl_add_u64 v[4:5], v[4:5], 0, v[146:147]
	s_mov_b64 s[36:37], -1
	s_and_b64 vcc, exec, s[8:9]
	global_store_dwordx2 v[4:5], v[2:3], off
	s_cbranch_vccnz .LBB0_1491
	s_and_b64 vcc, exec, s[6:7]
	s_cbranch_vccnz .LBB0_1490
	s_barrier
	s_branch .LBB0_1490
